# ssm_pre dt softplus loop: dtraw/dtf/dtb base pointers loaded once with scalar loads and selected per lane instead of dependent vector pointer loads every iteration
# baseline (speedup 1.0000x reference)
; __device__ void phase_ssm_pre(KParams& p, int bid, int nb, char* smem) {
;     ...
;   for (int i = bid * NTHREADS + tid; i < (T + TC) * 32; i += nb * NTHREADS) {
;     const bool isx = i < T * 32;
;     const int ii = isx ? i : i - T * 32;
;     const int t = ii >> 5, j = ii & 31;
;     const float v = (isx ? p.dtraw : p.dtraw_c)[ii];
;     float* df = isx ? p.dtf : p.dtf_c;
;     float* db = isx ? p.dtb : p.dtb_c;
.LBB0_666:
	s_mov_b32 s6, 0x48000
	v_cmp_gt_i32_e32 vcc, s6, v134
	s_and_saveexec_b64 s[12:13], vcc
	s_cbranch_execz .LBB0_677
	s_load_dwordx4 s[8:11], s[14:15], 0x70
	s_load_dwordx8 s[56:63], s[14:15], 0x1c0
	s_load_dwordx4 s[64:67], s[14:15], 0x1e0
	s_lshl_b32 s22, s34, 8
	s_mov_b64 s[16:17], 0
	s_mov_b32 s23, 0x40000
	v_mov_b32_e32 v10, 0x1c8
	v_mov_b32_e32 v11, 0x1c0
	s_waitcnt lgkmcnt(0)
	v_mov_b32_e32 v40, s56
	v_mov_b32_e32 v41, s57
	v_mov_b32_e32 v42, s60
	v_mov_b32_e32 v43, s61
	v_mov_b32_e32 v44, s62
	v_mov_b32_e32 v45, s63
	v_mov_b32_e32 v46, s58
	v_mov_b32_e32 v47, s59
	v_mov_b32_e32 v48, s64
	v_mov_b32_e32 v49, s65
	v_mov_b32_e32 v50, s66
	v_mov_b32_e32 v51, s67
	v_mov_b32_e32 v3, 0
	s_mov_b32 s24, 0x41a00000
	s_mov_b32 s25, 0x3f2aaaab
	v_mov_b32_e32 v12, 0x3ecc95a3
	s_mov_b32 s26, 0x3f317218
	s_mov_b32 s27, 0x7f800000
	s_mov_b32 s28, 0x33800000
	s_mov_b32 s29, 0x47fff
	v_mov_b32_e32 v13, 0x1e8
	v_mov_b32_e32 v14, 0x1d8
	v_mov_b32_e32 v4, 0x3f317218
	v_mov_b32_e32 v15, 0x7f800000
	v_mov_b32_e32 v16, 0x7fc00000
	v_mov_b32_e32 v17, 0xff800000
	v_mov_b32_e32 v18, 0x1e0
	v_mov_b32_e32 v19, 0x1d0
	s_branch .LBB0_670

; __device__ __forceinline__ float softplus_f(float v) { return v > 20.f ? v : log1pf(__expf(v)); }
; __device__ void phase_ssm_pre(KParams& p, int bid, int nb, char* smem) {
;     ...
;   for (int i = bid * NTHREADS + tid; i < (T + TC) * 32; i += nb * NTHREADS) {
;     const bool isx = i < T * 32;
;     const int ii = isx ? i : i - T * 32;
;     const int t = ii >> 5, j = ii & 31;
;     const float v = (isx ? p.dtraw : p.dtraw_c)[ii];
;     float* df = isx ? p.dtf : p.dtf_c;
;     float* db = isx ? p.dtb : p.dtb_c;
;     if (j < 16) df[t * 16 + j] = softplus_f(v + p.dt_bias_f[j]);
.LBB0_670:
	v_add_u32_e32 v2, 0xfffc0000, v134
	v_cmp_gt_i32_e32 vcc, s23, v134
	s_nop 1
	v_cndmask_b32_e32 v6, v2, v134, vcc
	v_cndmask_b32_e32 v8, v46, v40, vcc
	v_cndmask_b32_e32 v9, v47, v41, vcc
	v_ashrrev_i32_e32 v7, 31, v6
	v_and_b32_e32 v20, 31, v6
	v_cmp_lt_u32_e64 s[6:7], 15, v20
	v_lshl_add_u64 v[8:9], v[6:7], 2, v[8:9]
	global_load_dword v21, v[8:9], off
	v_ashrrev_i32_e32 v9, 5, v6
	s_and_saveexec_b64 s[18:19], s[6:7]
	s_xor_b64 s[18:19], exec, s[18:19]
	s_cbranch_execz .LBB0_674
	v_cndmask_b32_e32 v6, v50, v44, vcc
	v_cndmask_b32_e32 v7, v51, v45, vcc
	v_add_u32_e32 v2, -16, v20
	v_lshl_add_u64 v[24:25], v[2:3], 2, s[10:11]
	global_load_dword v5, v[24:25], off
	s_waitcnt vmcnt(0)
	v_add_f32_e32 v5, v21, v5
	v_cmp_nlt_f32_e64 s[6:7], s24, v5
	s_and_saveexec_b64 s[20:21], s[6:7]
	s_cbranch_execz .LBB0_673
	v_mul_f32_e32 v5, 0x3fb8aa3b, v5
	v_exp_f32_e32 v8, v5
	s_nop 0
	v_add_f32_e32 v5, 1.0, v8
	v_frexp_mant_f32_e32 v23, v5
	v_cvt_f64_f32_e32 v[20:21], v5
	v_add_f32_e32 v22, -1.0, v5
	v_frexp_exp_i32_f64_e32 v20, v[20:21]
	v_cmp_gt_f32_e64 s[6:7], s25, v23
	v_sub_f32_e32 v24, v22, v5
	v_sub_f32_e32 v22, v8, v22
	v_subbrev_co_u32_e64 v28, s[6:7], 0, v20, s[6:7]
	v_add_f32_e32 v24, 1.0, v24
	v_sub_u32_e32 v20, 0, v28
	v_add_f32_e32 v22, v22, v24
	v_ldexp_f32 v5, v5, v20
	v_ldexp_f32 v20, v22, v20
	v_add_f32_e32 v22, -1.0, v5
	v_add_f32_e32 v21, 1.0, v22
	v_sub_f32_e32 v21, v5, v21
	v_add_f32_e32 v23, v20, v21
	v_add_f32_e32 v21, 1.0, v5
	v_add_f32_e32 v24, -1.0, v21
	v_sub_f32_e32 v5, v5, v24
	v_add_f32_e32 v5, v20, v5
	v_add_f32_e32 v29, v21, v5
	v_rcp_f32_e32 v30, v29
	v_sub_f32_e32 v20, v29, v21
	v_add_f32_e32 v21, v22, v23
	v_sub_f32_e32 v5, v5, v20
	v_mul_f32_e32 v32, v21, v30
	v_sub_f32_e32 v20, v21, v22
	v_mul_f32_e32 v22, v29, v32
	v_fma_f32 v24, v32, v29, -v22
	v_fmac_f32_e32 v24, v32, v5
	v_sub_f32_e32 v31, v23, v20
	v_add_f32_e32 v20, v22, v24
	v_sub_f32_e32 v23, v21, v20
	v_pk_add_f32 v[26:27], v[20:21], v[22:23] neg_lo:[0,1] neg_hi:[0,1]
	v_mov_b32_e32 v25, v20
	v_pk_add_f32 v[20:21], v[26:27], v[24:25] neg_lo:[0,1] neg_hi:[0,1]
	v_cmp_neq_f32_e64 s[6:7], s27, v8
	v_add_f32_e32 v21, v31, v21
	v_add_f32_e32 v20, v20, v21
	v_add_f32_e32 v21, v23, v20
	v_mul_f32_e32 v31, v30, v21
	v_mul_f32_e32 v22, v29, v31
	v_fma_f32 v24, v31, v29, -v22
	v_fmac_f32_e32 v24, v31, v5
	v_sub_f32_e32 v5, v23, v21
	v_add_f32_e32 v5, v20, v5
	v_add_f32_e32 v20, v22, v24
	v_sub_f32_e32 v23, v21, v20
	v_pk_add_f32 v[26:27], v[20:21], v[22:23] neg_lo:[0,1] neg_hi:[0,1]
	v_mov_b32_e32 v25, v20
	v_pk_add_f32 v[20:21], v[26:27], v[24:25] neg_lo:[0,1] neg_hi:[0,1]
	s_nop 0
	v_add_f32_e32 v5, v5, v21
	v_add_f32_e32 v5, v20, v5
	v_add_f32_e32 v21, v32, v31
	v_add_f32_e32 v5, v23, v5
	v_sub_f32_e32 v20, v21, v32
	v_mul_f32_e32 v5, v30, v5
	v_sub_f32_e32 v20, v31, v20
	v_add_f32_e32 v22, v20, v5
	v_add_f32_e32 v24, v21, v22
	v_cvt_f32_i32_e32 v20, v28
	v_mul_f32_e32 v25, v24, v24
	v_sub_f32_e32 v21, v24, v21
	v_fmamk_f32 v5, v25, 0x3e9b6dac, v12
	v_sub_f32_e32 v21, v22, v21
	v_fmaak_f32 v5, v25, v5, 0x3f2aaada
	v_ldexp_f32 v26, v21, 1
	v_mul_f32_e32 v21, v24, v25
	v_ldexp_f32 v23, v24, 1
	v_pk_mul_f32 v[24:25], v[20:21], v[4:5]
	s_nop 0
	v_fma_f32 v22, v20, s26, -v24
	v_fmac_f32_e32 v22, 0xb102e308, v20
	v_pk_add_f32 v[20:21], v[24:25], v[22:23]
	s_nop 0
	v_sub_f32_e32 v5, v21, v23
	v_sub_f32_e32 v5, v25, v5
	v_add_f32_e32 v27, v26, v5
	v_mov_b32_e32 v26, v24
	v_pk_add_f32 v[24:25], v[20:21], v[24:25] neg_lo:[0,1] neg_hi:[0,1]
	v_pk_add_f32 v[28:29], v[20:21], v[26:27]
	v_mov_b32_e32 v23, v20
	v_mov_b32_e32 v25, v29
	v_pk_add_f32 v[30:31], v[22:23], v[24:25] neg_lo:[0,1] neg_hi:[0,1]
	v_pk_add_f32 v[22:23], v[22:23], v[24:25]
	v_mov_b32_e32 v26, v27
	v_pk_add_f32 v[24:25], v[22:23], v[20:21] op_sel:[1,0] op_sel_hi:[0,1] neg_lo:[0,1] neg_hi:[0,1]
	v_pk_add_f32 v[32:33], v[28:29], v[24:25] op_sel_hi:[1,0] neg_lo:[0,1] neg_hi:[0,1]
	v_mov_b32_e32 v28, v29
	v_mov_b32_e32 v29, v23
	v_pk_mov_b32 v[24:25], v[20:21], v[24:25] op_sel:[1,0]
	v_mov_b32_e32 v27, v20
	v_pk_add_f32 v[24:25], v[28:29], v[24:25] neg_lo:[0,1] neg_hi:[0,1]
	v_mov_b32_e32 v32, v30
	v_pk_add_f32 v[20:21], v[26:27], v[24:25] neg_lo:[0,1] neg_hi:[0,1]
	v_mov_b32_e32 v31, v23
	v_pk_add_f32 v[24:25], v[32:33], v[20:21]
	s_nop 0
	v_pk_add_f32 v[26:27], v[24:25], v[24:25] op_sel:[0,1] op_sel_hi:[1,0]
	s_nop 0
	v_pk_add_f32 v[22:23], v[22:23], v[26:27] op_sel:[1,0] op_sel_hi:[0,1]
	v_mov_b32_e32 v25, v22
	v_pk_add_f32 v[28:29], v[24:25], v[30:31] neg_lo:[0,1] neg_hi:[0,1]
	v_mov_b32_e32 v21, v26
	v_sub_f32_e32 v5, v24, v28
	v_pk_add_f32 v[20:21], v[20:21], v[28:29] neg_lo:[0,1] neg_hi:[0,1]
	v_sub_f32_e32 v5, v30, v5
	v_add_f32_e32 v5, v20, v5
	v_add_f32_e32 v5, v5, v21
	v_add_f32_e32 v5, v22, v5
	v_cndmask_b32_e64 v5, v15, v5, s[6:7]
	v_cmp_ngt_f32_e64 s[6:7], -1.0, v8
	s_nop 1
	v_cndmask_b32_e64 v5, v16, v5, s[6:7]
	v_cmp_neq_f32_e64 s[6:7], -1.0, v8
	s_nop 1
	v_cndmask_b32_e64 v5, v17, v5, s[6:7]
	v_cmp_lt_f32_e64 s[6:7], |v8|, s28
	s_nop 1
	v_cndmask_b32_e64 v5, v5, v8, s[6:7]

; __device__ __forceinline__ float softplus_f(float v) { return v > 20.f ? v : log1pf(__expf(v)); }
; __device__ void phase_ssm_pre(KParams& p, int bid, int nb, char* smem) {
;     ...
;     const float v = (isx ? p.dtraw : p.dtraw_c)[ii];
;     float* df = isx ? p.dtf : p.dtf_c;
;     float* db = isx ? p.dtb : p.dtb_c;
;     if (j < 16) df[t * 16 + j] = softplus_f(v + p.dt_bias_f[j]);
.LBB0_674:
	s_andn2_saveexec_b64 s[6:7], s[18:19]
	s_cbranch_execz .LBB0_669
	v_lshlrev_b32_e32 v5, 2, v20
	v_cndmask_b32_e32 v6, v48, v42, vcc
	v_cndmask_b32_e32 v7, v49, v43, vcc
	global_load_dword v5, v5, s[8:9]
	s_waitcnt vmcnt(0)
	v_add_f32_e32 v5, v21, v5
	v_cmp_nlt_f32_e32 vcc, s24, v5
	s_and_saveexec_b64 s[18:19], vcc
	s_cbranch_execz .LBB0_668
	v_mul_f32_e32 v2, 0x3fb8aa3b, v5
	v_exp_f32_e32 v2, v2
	s_nop 0
	v_add_f32_e32 v5, 1.0, v2
	v_frexp_mant_f32_e32 v21, v5
	v_cvt_f64_f32_e32 v[22:23], v5
	v_add_f32_e32 v8, -1.0, v5
	v_frexp_exp_i32_f64_e32 v22, v[22:23]
	v_cmp_gt_f32_e32 vcc, s25, v21
	v_sub_f32_e32 v24, v8, v5
	v_sub_f32_e32 v8, v2, v8
	v_subbrev_co_u32_e32 v21, vcc, 0, v22, vcc
	v_add_f32_e32 v24, 1.0, v24
	v_sub_u32_e32 v22, 0, v21
	v_add_f32_e32 v8, v8, v24
	v_ldexp_f32 v5, v5, v22
	v_ldexp_f32 v8, v8, v22
	v_add_f32_e32 v22, -1.0, v5
	v_add_f32_e32 v23, 1.0, v22
	v_sub_f32_e32 v23, v5, v23
	v_add_f32_e32 v24, v8, v23
	v_add_f32_e32 v23, 1.0, v5
	v_add_f32_e32 v25, -1.0, v23
	v_sub_f32_e32 v5, v5, v25
	v_add_f32_e32 v5, v8, v5
	v_add_f32_e32 v8, v23, v5
	v_rcp_f32_e32 v30, v8
	v_sub_f32_e32 v23, v8, v23
	v_sub_f32_e32 v5, v5, v23
	v_add_f32_e32 v23, v22, v24
	v_sub_f32_e32 v22, v23, v22
	v_mul_f32_e32 v32, v23, v30
	v_sub_f32_e32 v31, v24, v22
	v_mul_f32_e32 v24, v8, v32
	v_fma_f32 v26, v32, v8, -v24
	v_fmac_f32_e32 v26, v32, v5
	v_add_f32_e32 v22, v24, v26
	v_sub_f32_e32 v25, v23, v22
	v_pk_add_f32 v[28:29], v[22:23], v[24:25] neg_lo:[0,1] neg_hi:[0,1]
	v_mov_b32_e32 v27, v22
	v_pk_add_f32 v[22:23], v[28:29], v[26:27] neg_lo:[0,1] neg_hi:[0,1]
	v_cmp_neq_f32_e32 vcc, s27, v2
	v_add_f32_e32 v23, v31, v23
	v_add_f32_e32 v22, v22, v23
	v_add_f32_e32 v23, v25, v22
	v_mul_f32_e32 v31, v30, v23
	v_mul_f32_e32 v24, v8, v31
	v_fma_f32 v26, v31, v8, -v24
	v_fmac_f32_e32 v26, v31, v5
	v_sub_f32_e32 v5, v25, v23
	v_add_f32_e32 v5, v22, v5
	v_add_f32_e32 v22, v24, v26
	v_sub_f32_e32 v25, v23, v22
	v_pk_add_f32 v[28:29], v[22:23], v[24:25] neg_lo:[0,1] neg_hi:[0,1]
	v_mov_b32_e32 v27, v22
	v_pk_add_f32 v[22:23], v[28:29], v[26:27] neg_lo:[0,1] neg_hi:[0,1]
	v_add_f32_e32 v8, v32, v31
	v_add_f32_e32 v5, v5, v23
	v_add_f32_e32 v5, v22, v5
	v_add_f32_e32 v5, v25, v5
	v_sub_f32_e32 v22, v8, v32
	v_mul_f32_e32 v5, v30, v5
	v_sub_f32_e32 v22, v31, v22
	v_add_f32_e32 v23, v22, v5
	v_add_f32_e32 v24, v8, v23
	v_cvt_f32_i32_e32 v22, v21
	v_mul_f32_e32 v26, v24, v24
	v_fmamk_f32 v5, v26, 0x3e9b6dac, v12
	v_sub_f32_e32 v8, v24, v8
	v_fmaak_f32 v5, v26, v5, 0x3f2aaada
	v_sub_f32_e32 v8, v23, v8
	v_mul_f32_e32 v23, v24, v26
	v_pk_mul_f32 v[26:27], v[22:23], v[4:5]
	v_ldexp_f32 v25, v24, 1
	v_fma_f32 v24, v22, s26, -v26
	v_fmac_f32_e32 v24, 0xb102e308, v22
	v_pk_add_f32 v[22:23], v[26:27], v[24:25]
	v_ldexp_f32 v8, v8, 1
	v_sub_f32_e32 v5, v23, v25
	v_sub_f32_e32 v5, v27, v5
	v_add_f32_e32 v29, v8, v5
	v_mov_b32_e32 v28, v26
	v_pk_add_f32 v[26:27], v[22:23], v[26:27] neg_lo:[0,1] neg_hi:[0,1]
	v_pk_add_f32 v[30:31], v[22:23], v[28:29]
	v_mov_b32_e32 v25, v22
	v_mov_b32_e32 v27, v31
	v_pk_add_f32 v[32:33], v[24:25], v[26:27] neg_lo:[0,1] neg_hi:[0,1]
	v_pk_add_f32 v[24:25], v[24:25], v[26:27]
	v_mov_b32_e32 v28, v29
	v_pk_add_f32 v[26:27], v[24:25], v[22:23] op_sel:[1,0] op_sel_hi:[0,1] neg_lo:[0,1] neg_hi:[0,1]
	v_pk_add_f32 v[34:35], v[30:31], v[26:27] op_sel_hi:[1,0] neg_lo:[0,1] neg_hi:[0,1]
	v_mov_b32_e32 v30, v31
	v_mov_b32_e32 v31, v25
	v_pk_mov_b32 v[26:27], v[22:23], v[26:27] op_sel:[1,0]
	v_mov_b32_e32 v29, v22
	v_pk_add_f32 v[26:27], v[30:31], v[26:27] neg_lo:[0,1] neg_hi:[0,1]
	v_mov_b32_e32 v34, v32
	v_pk_add_f32 v[22:23], v[28:29], v[26:27] neg_lo:[0,1] neg_hi:[0,1]
	v_mov_b32_e32 v33, v25
	v_pk_add_f32 v[26:27], v[34:35], v[22:23]
	s_nop 0
	v_pk_add_f32 v[28:29], v[26:27], v[26:27] op_sel:[0,1] op_sel_hi:[1,0]
	s_nop 0
	v_pk_add_f32 v[24:25], v[24:25], v[28:29] op_sel:[1,0] op_sel_hi:[0,1]
	v_mov_b32_e32 v27, v24
	v_pk_add_f32 v[30:31], v[26:27], v[32:33] neg_lo:[0,1] neg_hi:[0,1]
	v_mov_b32_e32 v23, v28
	v_sub_f32_e32 v5, v26, v30
	v_pk_add_f32 v[22:23], v[22:23], v[30:31] neg_lo:[0,1] neg_hi:[0,1]
	v_sub_f32_e32 v5, v32, v5
	v_add_f32_e32 v5, v22, v5
	v_add_f32_e32 v5, v5, v23
	v_add_f32_e32 v5, v24, v5
	v_cndmask_b32_e32 v5, v15, v5, vcc
	v_cmp_ngt_f32_e32 vcc, -1.0, v2
	s_nop 1
	v_cndmask_b32_e32 v5, v16, v5, vcc
	v_cmp_neq_f32_e32 vcc, -1.0, v2
	s_nop 1
	v_cndmask_b32_e32 v5, v17, v5, vcc
	v_cmp_lt_f32_e64 vcc, |v2|, s28
	s_nop 1
	v_cndmask_b32_e32 v5, v5, v2, vcc
	s_branch .LBB0_668
